# mixer gated-norm items: 32-lane sums of squares via DPP + one permlane16 swap instead of five dependent ds_bpermute round trips per row pair
# speedup vs baseline: 1.0004x; 1.0004x over previous
; __device__ __forceinline__ float bflo(unsigned w) { return __uint_as_float(w << 16); }
; __device__ __forceinline__ float bfhi(unsigned w) { return __uint_as_float(w & 0xffff0000u); }
; __device__ __forceinline__ float shx(float v, int m, int lane) { return __int_as_float(__builtin_amdgcn_ds_bpermute((lane ^ m) << 2, __float_as_int(v))); }
; __device__ __forceinline__ void p5_item(const Frame& F, int layer, int rbeg) {
;     ...
;         for (int q = 0; q < 2; ++q) { const int row = r0 + q;
;             float g[8]; float ss = 0.f;
; #pragma unroll
;             for (int i = 0; i < 4; ++i) {
;                 const float y0 = bflo(yf[q][i]) + bflo(yb[q][i]) + dsk * bflo(xs[q][i]), y1 = bfhi(yf[q][i]) + bfhi(yb[q][i]) + dsk * bfhi(xs[q][i]);
;                 const float z0 = bflo(z[q][i]), z1 = bfhi(z[q][i]);
;                 g[2 * i] = y0 * z0 * __builtin_amdgcn_rcpf(1.f + __expf(-z0)); g[2 * i + 1] = y1 * z1 * __builtin_amdgcn_rcpf(1.f + __expf(-z1)); ss += g[2 * i] * g[2 * i] + g[2 * i + 1] * g[2 * i + 1]; }
; #pragma unroll
;             for (int o = 1; o < 32; o <<= 1) ss += shx(ss, o, lane);
.LBB0_634:
	v_lshlrev_b32_e32 v96, 16, v60
	v_and_b32_e32 v97, 0xffff0000, v60
	v_lshlrev_b32_e32 v98, 16, v61
	v_and_b32_e32 v99, 0xffff0000, v61
	v_lshlrev_b32_e32 v60, 16, v70
	v_and_b32_e32 v61, 0xffff0000, v70
	v_lshlrev_b32_e32 v100, 16, v66
	v_and_b32_e32 v101, 0xffff0000, v66
	v_lshlrev_b32_e32 v70, 16, v71
	v_and_b32_e32 v71, 0xffff0000, v71
	v_lshlrev_b32_e32 v66, 16, v67
	v_and_b32_e32 v67, 0xffff0000, v67
	v_lshlrev_b32_e32 v102, 16, v62
	v_and_b32_e32 v103, 0xffff0000, v62
	v_lshlrev_b32_e32 v62, 16, v63
	v_and_b32_e32 v63, 0xffff0000, v63
	v_pk_add_f32 v[66:67], v[66:67], v[70:71]
	v_pk_add_f32 v[60:61], v[100:101], v[60:61]
	v_pk_fma_f32 v[62:63], v[74:75], v[62:63], v[66:67]
	v_lshlrev_b32_e32 v66, 16, v59
	v_mul_f32_e32 v67, 0xbfb8aa3b, v66
	v_exp_f32_e32 v70, v67
	v_and_b32_e32 v67, 0xffff0000, v59
	v_mul_f32_e32 v59, 0xbfb8aa3b, v67
	v_exp_f32_e32 v59, v59
	v_pk_mul_f32 v[62:63], v[62:63], v[66:67]
	v_lshlrev_b32_e32 v66, 16, v58
	v_and_b32_e32 v67, 0xffff0000, v58
	v_mul_f32_e32 v58, 0xbfb8aa3b, v66
	v_add_f32_e32 v70, 1.0, v70
	v_add_f32_e32 v59, 1.0, v59
	v_exp_f32_e32 v91, v58
	v_mul_f32_e32 v58, 0xbfb8aa3b, v67
	v_rcp_f32_e32 v70, v70
	v_rcp_f32_e32 v71, v59
	v_exp_f32_e32 v104, v58
	v_pk_fma_f32 v[60:61], v[74:75], v[102:103], v[60:61]
	v_lshlrev_b32_e32 v92, 16, v68
	v_pk_mul_f32 v[58:59], v[62:63], v[70:71]
	v_add_f32_e32 v62, 1.0, v91
	v_add_f32_e32 v63, 1.0, v104
	v_rcp_f32_e32 v62, v62
	v_rcp_f32_e32 v63, v63
	v_pk_mul_f32 v[60:61], v[60:61], v[66:67]
	v_mov_b32_e32 v66, v59
	v_and_b32_e32 v93, 0xffff0000, v68
	v_pk_mul_f32 v[60:61], v[60:61], v[62:63]
	v_mov_b32_e32 v62, v58
	v_mov_b32_e32 v63, v60
	v_pk_mul_f32 v[62:63], v[62:63], v[62:63]
	v_mov_b32_e32 v67, v61
	v_pk_fma_f32 v[62:63], v[66:67], v[66:67], v[62:63]
	v_lshlrev_b32_e32 v66, 16, v57
	v_lshlrev_b32_e32 v94, 16, v64
	v_and_b32_e32 v95, 0xffff0000, v64
	v_lshlrev_b32_e32 v68, 16, v69
	v_and_b32_e32 v69, 0xffff0000, v69
	v_lshlrev_b32_e32 v64, 16, v65
	v_and_b32_e32 v65, 0xffff0000, v65
	v_mul_f32_e32 v67, 0xbfb8aa3b, v66
	v_pk_add_f32 v[64:65], v[64:65], v[68:69]
	v_exp_f32_e32 v68, v67
	v_and_b32_e32 v67, 0xffff0000, v57
	v_mul_f32_e32 v57, 0xbfb8aa3b, v67
	v_exp_f32_e32 v57, v57
	v_pk_fma_f32 v[64:65], v[74:75], v[98:99], v[64:65]
	v_add_f32_e32 v68, 1.0, v68
	v_pk_mul_f32 v[64:65], v[64:65], v[66:67]
	v_lshlrev_b32_e32 v66, 16, v56
	v_and_b32_e32 v67, 0xffff0000, v56
	v_mul_f32_e32 v56, 0xbfb8aa3b, v66
	v_add_f32_e32 v57, 1.0, v57
	v_exp_f32_e32 v70, v56
	v_mul_f32_e32 v56, 0xbfb8aa3b, v67
	v_rcp_f32_e32 v68, v68
	v_rcp_f32_e32 v69, v57
	v_exp_f32_e32 v71, v56
	v_lshlrev_b32_e32 v98, 16, v46
	v_and_b32_e32 v99, 0xffff0000, v46
	v_pk_mul_f32 v[56:57], v[64:65], v[68:69]
	v_add_f32_e32 v64, 1.0, v70
	v_add_f32_e32 v65, 1.0, v71
	v_rcp_f32_e32 v64, v64
	v_rcp_f32_e32 v65, v65
	v_pk_add_f32 v[68:69], v[94:95], v[92:93]
	v_lshlrev_b32_e32 v70, 16, v48
	v_pk_fma_f32 v[68:69], v[74:75], v[96:97], v[68:69]
	v_and_b32_e32 v71, 0xffff0000, v48
	v_pk_mul_f32 v[66:67], v[68:69], v[66:67]
	v_mov_b32_e32 v69, v57
	v_pk_mul_f32 v[64:65], v[66:67], v[64:65]
	v_mov_b32_e32 v67, v56
	v_mov_b32_e32 v66, v64
	v_pk_mul_f32 v[66:67], v[66:67], v[66:67]
	v_mov_b32_e32 v68, v65
	v_pk_fma_f32 v[66:67], v[68:69], v[68:69], v[66:67]
	v_lshlrev_b32_e32 v68, 16, v52
	v_and_b32_e32 v69, 0xffff0000, v52
	v_lshlrev_b32_e32 v52, 16, v53
	v_and_b32_e32 v53, 0xffff0000, v53
	v_lshlrev_b32_e32 v48, 16, v49
	v_and_b32_e32 v49, 0xffff0000, v49
	v_lshlrev_b32_e32 v92, 16, v44
	v_and_b32_e32 v93, 0xffff0000, v44
	v_lshlrev_b32_e32 v44, 16, v45
	v_and_b32_e32 v45, 0xffff0000, v45
	v_lshlrev_b32_e32 v94, 16, v54
	v_and_b32_e32 v95, 0xffff0000, v54
	v_lshlrev_b32_e32 v96, 16, v50
	v_and_b32_e32 v97, 0xffff0000, v50
	v_lshlrev_b32_e32 v54, 16, v55
	v_and_b32_e32 v55, 0xffff0000, v55
	v_lshlrev_b32_e32 v50, 16, v51
	v_and_b32_e32 v51, 0xffff0000, v51
	v_pk_add_f32 v[48:49], v[48:49], v[52:53]
	v_lshlrev_b32_e32 v46, 16, v47
	v_and_b32_e32 v47, 0xffff0000, v47
	v_pk_add_f32 v[50:51], v[50:51], v[54:55]
	v_pk_fma_f32 v[44:45], v[74:75], v[44:45], v[48:49]
	v_lshlrev_b32_e32 v48, 16, v41
	v_pk_fma_f32 v[46:47], v[74:75], v[46:47], v[50:51]
	v_lshlrev_b32_e32 v50, 16, v43
	v_mul_f32_e32 v49, 0xbfb8aa3b, v48
	v_mul_f32_e32 v51, 0xbfb8aa3b, v50
	v_exp_f32_e32 v52, v49
	v_and_b32_e32 v49, 0xffff0000, v41
	v_exp_f32_e32 v54, v51
	v_and_b32_e32 v51, 0xffff0000, v43
	v_mul_f32_e32 v41, 0xbfb8aa3b, v49
	v_mul_f32_e32 v43, 0xbfb8aa3b, v51
	v_exp_f32_e32 v41, v41
	v_exp_f32_e32 v43, v43
	v_pk_mul_f32 v[44:45], v[44:45], v[48:49]
	v_lshlrev_b32_e32 v48, 16, v40
	v_add_f32_e32 v41, 1.0, v41
	v_and_b32_e32 v49, 0xffff0000, v40
	v_pk_mul_f32 v[46:47], v[46:47], v[50:51]
	v_add_f32_e32 v43, 1.0, v43
	v_lshlrev_b32_e32 v50, 16, v42
	v_and_b32_e32 v51, 0xffff0000, v42
	v_rcp_f32_e32 v53, v41
	v_mul_f32_e32 v40, 0xbfb8aa3b, v48
	v_mul_f32_e32 v41, 0xbfb8aa3b, v49
	v_rcp_f32_e32 v55, v43
	v_mul_f32_e32 v42, 0xbfb8aa3b, v50
	v_mul_f32_e32 v43, 0xbfb8aa3b, v51
	v_exp_f32_e32 v40, v40
	v_exp_f32_e32 v41, v41
	v_exp_f32_e32 v42, v42
	v_exp_f32_e32 v43, v43
	v_add_f32_e32 v52, 1.0, v52
	v_add_f32_e32 v54, 1.0, v54
	v_rcp_f32_e32 v52, v52
	v_rcp_f32_e32 v54, v54
	v_add_f32_e32 v40, 1.0, v40
	v_add_f32_e32 v41, 1.0, v41
	v_add_f32_e32 v42, 1.0, v42
	v_add_f32_e32 v43, 1.0, v43
	v_rcp_f32_e32 v40, v40
	v_rcp_f32_e32 v41, v41
	v_rcp_f32_e32 v42, v42
	v_rcp_f32_e32 v43, v43
	v_pk_mul_f32 v[44:45], v[52:53], v[44:45]
	v_pk_add_f32 v[52:53], v[70:71], v[68:69]
	v_pk_mul_f32 v[46:47], v[54:55], v[46:47]
	v_pk_add_f32 v[54:55], v[96:97], v[94:95]
	v_pk_fma_f32 v[52:53], v[74:75], v[92:93], v[52:53]
	v_pk_fma_f32 v[54:55], v[74:75], v[98:99], v[54:55]
	v_pk_mul_f32 v[48:49], v[52:53], v[48:49]
	v_pk_mul_f32 v[50:51], v[54:55], v[50:51]
	v_pk_mul_f32 v[48:49], v[40:41], v[48:49]
	v_pk_mul_f32 v[50:51], v[42:43], v[50:51]
	v_mov_b32_e32 v40, v48
	v_mov_b32_e32 v41, v44
	v_mov_b32_e32 v42, v46
	v_mov_b32_e32 v43, v50
	v_pk_mul_f32 v[40:41], v[40:41], v[40:41]
	v_mov_b32_e32 v52, v49
	v_mov_b32_e32 v53, v45
	v_pk_mul_f32 v[42:43], v[42:43], v[42:43]
	v_mov_b32_e32 v54, v47
	v_mov_b32_e32 v55, v51
	v_pk_fma_f32 v[40:41], v[52:53], v[52:53], v[40:41]
	v_pk_fma_f32 v[42:43], v[54:55], v[54:55], v[42:43]
	v_mov_b32_e32 v52, v40
	v_mov_b32_e32 v53, v66
	v_mov_b32_e32 v66, v41
	v_pk_add_f32 v[40:41], v[52:53], v[66:67]
	v_mov_b32_e32 v52, v43
	v_mov_b32_e32 v53, v63
	v_pk_add_f32 v[40:41], v[52:53], v[40:41]
	v_mov_b32_e32 v43, v62
	v_pk_add_f32 v[40:41], v[42:43], v[40:41]
	s_mov_b32 s12, 0x3b800000
	s_waitcnt vmcnt(7)
; __device__ __forceinline__ unsigned pk2(float lo, float hi) { f32x2_t v = {lo, hi}; bf16x2_t b = __builtin_convertvector(v, bf16x2_t); return __builtin_bit_cast(unsigned, b); }
; __device__ __forceinline__ float shx(float v, int m, int lane) { return __int_as_float(__builtin_amdgcn_ds_bpermute((lane ^ m) << 2, __float_as_int(v))); }
; __device__ __forceinline__ void p5_item(const Frame& F, int layer, int rbeg) {
;     ...
;             for (int o = 1; o < 32; o <<= 1) ss += shx(ss, o, lane);
;             const float rstd = rsqrtf(ss * (1.f / 256.f) + EPS);
;             u32x4 o; o.x = pk2(g[0] * rstd * w0[0], g[1] * rstd * w0[1]); o.y = pk2(g[2] * rstd * w0[2], g[3] * rstd * w0[3]);
;             o.z = pk2(g[4] * rstd * w1[0], g[5] * rstd * w1[1]); o.w = pk2(g[6] * rstd * w1[2], g[7] * rstd * w1[3]);
;             *(u32x4*)(A2p + (size_t)row * 1024 + 512 + c0) = o; }
	v_mov_b64_e32 v[70:71], v[14:15]
	v_mov_b64_e32 v[68:69], v[12:13]
	s_nop 0
	v_add_f32_dpp v40, v40, v40 quad_perm:[1,0,3,2] row_mask:0xf bank_mask:0xf
	v_add_f32_dpp v41, v41, v41 quad_perm:[1,0,3,2] row_mask:0xf bank_mask:0xf
	s_nop 0
	v_add_f32_dpp v40, v40, v40 quad_perm:[2,3,0,1] row_mask:0xf bank_mask:0xf
	v_add_f32_dpp v41, v41, v41 quad_perm:[2,3,0,1] row_mask:0xf bank_mask:0xf
	s_nop 0
	v_add_f32_dpp v40, v40, v40 row_half_mirror row_mask:0xf bank_mask:0xf
	v_add_f32_dpp v41, v41, v41 row_half_mirror row_mask:0xf bank_mask:0xf
	s_nop 0
	v_add_f32_dpp v40, v40, v40 row_mirror row_mask:0xf bank_mask:0xf
	v_add_f32_dpp v41, v41, v41 row_mirror row_mask:0xf bank_mask:0xf
	v_mov_b32_e32 v42, v40
	v_mov_b32_e32 v43, v41
	s_nop 1
	v_permlane16_swap_b32 v42, v40
	v_permlane16_swap_b32 v43, v41
	s_nop 0
	v_pk_add_f32 v[40:41], v[40:41], v[42:43]
	s_nop 0
	v_pk_fma_f32 v[52:53], v[40:41], s[12:13], v[246:247] op_sel_hi:[1,0,0]
	s_add_i32 s12, s4, 1
	v_mul_f32_e32 v40, 0x4b800000, v53
	v_cmp_gt_f32_e32 vcc, s22, v53
	s_ashr_i32 s13, s12, 31
	s_lshl_b64 s[12:13], s[12:13], 11
	v_cndmask_b32_e32 v40, v53, v40, vcc
	v_rsq_f32_e32 v40, v40
	s_add_u32 s12, s2, s12
	s_addc_u32 s13, s3, s13
	s_mov_b32 s4, s6
	v_mul_f32_e32 v41, 0x45800000, v40
	v_cndmask_b32_e32 v54, v40, v41, vcc
	v_pk_mul_f32 v[40:41], v[64:65], v[54:55] op_sel_hi:[1,0]
	v_pk_mul_f32 v[42:43], v[56:57], v[54:55] op_sel_hi:[1,0]
	v_pk_mul_f32 v[40:41], v[0:1], v[40:41]
	v_pk_mul_f32 v[42:43], v[2:3], v[42:43]
	v_cvt_pk_bf16_f32 v40, v40, v41
	v_cvt_pk_bf16_f32 v41, v42, v43
	v_pk_mul_f32 v[42:43], v[60:61], v[54:55] op_sel_hi:[1,0]
	v_cmp_gt_f32_e32 vcc, s22, v52
	v_pk_mul_f32 v[42:43], v[4:5], v[42:43]
	v_pk_mul_f32 v[54:55], v[58:59], v[54:55] op_sel_hi:[1,0]
	v_cvt_pk_bf16_f32 v42, v42, v43
	v_mul_f32_e32 v43, 0x4b800000, v52
	v_cndmask_b32_e32 v43, v52, v43, vcc
	v_rsq_f32_e32 v56, v43
	v_pk_mul_f32 v[52:53], v[6:7], v[54:55]
	s_waitcnt vmcnt(5)
	v_mov_b64_e32 v[66:67], v[10:11]
	v_cvt_pk_bf16_f32 v43, v52, v53
	global_store_dwordx4 v[84:85], v[40:43], off
	s_waitcnt vmcnt(5)
	v_mov_b64_e32 v[62:63], v[18:19]
	v_mov_b64_e32 v[64:65], v[8:9]
	v_mul_f32_e32 v40, 0x45800000, v56
	v_cndmask_b32_e32 v52, v56, v40, vcc
	v_pk_mul_f32 v[40:41], v[48:49], v[52:53] op_sel_hi:[1,0]
	v_pk_mul_f32 v[42:43], v[44:45], v[52:53] op_sel_hi:[1,0]
	v_pk_mul_f32 v[40:41], v[0:1], v[40:41]
	v_pk_mul_f32 v[42:43], v[2:3], v[42:43]
	v_cvt_pk_bf16_f32 v40, v40, v41
	v_cvt_pk_bf16_f32 v41, v42, v43
	v_pk_mul_f32 v[42:43], v[50:51], v[52:53] op_sel_hi:[1,0]
	v_pk_mul_f32 v[44:45], v[46:47], v[52:53] op_sel_hi:[1,0]
	v_pk_mul_f32 v[42:43], v[4:5], v[42:43]
	v_pk_mul_f32 v[44:45], v[6:7], v[44:45]
	v_cvt_pk_bf16_f32 v42, v42, v43
	v_cvt_pk_bf16_f32 v43, v44, v45
	v_lshl_add_u64 v[44:45], v[72:73], 1, s[12:13]
	v_add_co_u32_e32 v44, vcc, 0x46b34000, v44
	s_mov_b64 s[12:13], 0x8000
	s_nop 0
	v_addc_co_u32_e32 v45, vcc, 0, v45, vcc
	global_store_dwordx4 v[44:45], v[40:43], off offset:3072
	s_waitcnt vmcnt(4)
	v_mov_b64_e32 v[50:51], v[26:27]
	s_waitcnt vmcnt(3)
	v_mov_b64_e32 v[46:47], v[34:35]
	s_waitcnt vmcnt(2)
	v_mov_b64_e32 v[42:43], v[38:39]
	v_mov_b64_e32 v[58:59], v[22:23]
	v_mov_b64_e32 v[54:55], v[30:31]
	v_lshl_add_u64 v[84:85], v[84:85], 0, s[12:13]
	s_and_b64 vcc, exec, s[10:11]
	v_mov_b64_e32 v[48:49], v[24:25]
	v_mov_b64_e32 v[44:45], v[32:33]
	v_mov_b64_e32 v[60:61], v[16:17]
	v_mov_b64_e32 v[40:41], v[36:37]
	v_mov_b64_e32 v[56:57], v[20:21]
	v_mov_b64_e32 v[52:53], v[28:29]
	s_cbranch_vccnz .LBB0_637
